# R3 attention loop + workgroup-uniform fast/slow softmax-path decision (LDS flag) so mixed waves cannot split across the two LDS protocols
# baseline (speedup 1.0000x reference)
.LBB0_1138:
	v_mov_b32_e32 v224, 0
	s_mov_b32 s1, 0
	v_mov_b32_e32 v36, 0
	v_mov_b32_e32 v37, v224
	v_mov_b32_e32 v38, v224
	v_mov_b32_e32 v39, v224
	v_mov_b32_e32 v40, v224
	v_mov_b32_e32 v41, v224
	v_mov_b32_e32 v42, v224
	v_mov_b32_e32 v43, v224
	v_mov_b32_e32 v44, v224
	v_mov_b32_e32 v45, v224
	v_mov_b32_e32 v46, v224
	v_mov_b32_e32 v47, v224
	v_mov_b32_e32 v48, v224
	v_mov_b32_e32 v49, v224
	v_mov_b32_e32 v50, v224
	v_mov_b32_e32 v51, v224
	v_mov_b32_e32 v52, 0
	v_mov_b32_e32 v53, v224
	v_mov_b32_e32 v54, v224
	v_mov_b32_e32 v55, v224
	v_mov_b32_e32 v56, v224
	v_mov_b32_e32 v57, v224
	v_mov_b32_e32 v58, v224
	v_mov_b32_e32 v59, v224
	v_mov_b32_e32 v60, v224
	v_mov_b32_e32 v61, v224
	v_mov_b32_e32 v62, v224
	v_mov_b32_e32 v63, v224
	v_mov_b32_e32 v64, v224
	v_mov_b32_e32 v65, v224
	v_mov_b32_e32 v66, v224
	v_mov_b32_e32 v67, v224
.LBB0_1139:
	s_add_i32 s2, s23, s1
	s_add_i32 s0, s1, 2
	s_add_i32 s1, s2, 2
	s_add_i32 s3, s2, 1
	s_cmp_ge_u32 s1, s34
	s_cselect_b32 s7, s34, 0
	s_sub_i32 s12, s1, s7
	s_cmp_ge_i32 s12, s34
	s_cselect_b32 s12, s34, 0
	s_add_i32 s7, s7, s12
	s_sub_i32 s1, s1, s7
	s_cmp_ge_u32 s3, s34
	s_cselect_b32 s7, s34, 0
	s_sub_i32 s3, s3, s7
	s_cmp_ge_i32 s3, s34
	s_cselect_b32 s3, s34, 0
	s_add_i32 s7, s7, s3
	s_sub_i32 s3, s2, s7
	s_lshl_b32 s3, s3, 7
	v_lshl_add_u32 v68, s1, v215, v223
	global_load_dwordx4 v[100:103], v68, s[44:45]
	v_mad_u64_u32 v[68:69], s[12:13], s1, v199, v[202:203]
	s_addk_i32 s3, 0x80
	global_load_dwordx2 v[128:129], v68, s[44:45]
	v_add_u32_e32 v68, s3, v204
	global_load_dwordx4 v[104:107], v68, s[44:45]
	ds_read_b128 v[68:71], v205 offset:19968
	ds_read_b128 v[72:75], v205 offset:13312
	ds_read_b128 v[108:111], v205 offset:13344
	ds_read_b128 v[112:115], v205 offset:20000
	s_waitcnt lgkmcnt(2)
	v_mfma_f32_32x32x16_bf16 v[84:99], v[72:75], v[132:135], 0
	v_exp_f32_e32 v20, v20
	v_exp_f32_e32 v131, v4
	v_exp_f32_e32 v21, v21
	v_exp_f32_e32 v160, v5
	v_exp_f32_e32 v22, v22
	v_exp_f32_e32 v161, v6
	v_exp_f32_e32 v23, v23
	v_mfma_f32_32x32x16_bf16 v[68:83], v[68:71], v[132:135], 0
	v_exp_f32_e32 v162, v7
	v_exp_f32_e32 v24, v24
	v_exp_f32_e32 v163, v8
	v_exp_f32_e32 v25, v25
	v_exp_f32_e32 v164, v9
	v_exp_f32_e32 v26, v26
	v_exp_f32_e32 v165, v10
	s_waitcnt lgkmcnt(0)
	v_mfma_f32_32x32x16_bf16 v[68:83], v[112:115], v[136:139], v[68:83]
	v_exp_f32_e32 v27, v27
	v_exp_f32_e32 v166, v11
	v_exp_f32_e32 v28, v28
	v_exp_f32_e32 v29, v29
	v_exp_f32_e32 v30, v30
	v_exp_f32_e32 v31, v31
	v_add_u32_e32 v130, v218, v217
	v_mfma_f32_32x32x16_bf16 v[84:99], v[108:111], v[136:139], v[84:99]
	ds_read_b128 v[108:111], v205 offset:20032
	ds_read_b128 v[112:115], v205 offset:13376
	v_exp_f32_e32 v32, v32
	v_exp_f32_e32 v33, v33
	v_exp_f32_e32 v34, v34
	v_exp_f32_e32 v35, v35
	s_waitcnt lgkmcnt(1)
	v_mfma_f32_32x32x16_bf16 v[68:83], v[108:111], v[140:143], v[68:83]
	s_waitcnt lgkmcnt(0)
	v_mfma_f32_32x32x16_bf16 v[84:99], v[112:115], v[140:143], v[84:99]
	ds_read_b128 v[108:111], v205 offset:20064
	ds_read_b128 v[112:115], v205 offset:13408
	ds_read_b128 v[116:119], v205 offset:13440
	s_waitcnt lgkmcnt(2)
	v_mfma_f32_32x32x16_bf16 v[68:83], v[108:111], v[144:147], v[68:83]
	ds_read_b128 v[108:111], v205 offset:20096
	s_waitcnt lgkmcnt(0)
	v_mfma_f32_32x32x16_bf16 v[68:83], v[108:111], v[148:151], v[68:83]
	v_mfma_f32_32x32x16_bf16 v[84:99], v[112:115], v[144:147], v[84:99]
	ds_read_b128 v[108:111], v205 offset:20128
	ds_read_b128 v[112:115], v205 offset:13472
	s_waitcnt lgkmcnt(1)
	v_mfma_f32_32x32x16_bf16 v[68:83], v[108:111], v[152:155], v[68:83]
	v_add_f32_e32 v108, 0, v20
	v_add_f32_e32 v4, v131, v108
	v_add_f32_e32 v4, v21, v4
	v_add_f32_e32 v4, v160, v4
	v_add_f32_e32 v4, v22, v4
	v_add_f32_e32 v4, v161, v4
	v_add_f32_e32 v4, v23, v4
	v_add_f32_e32 v4, v162, v4
	v_add_f32_e32 v4, v24, v4
	v_mfma_f32_32x32x16_bf16 v[84:99], v[116:119], v[148:151], v[84:99]
	v_add_f32_e32 v4, v163, v4
	v_add_f32_e32 v4, v25, v4
	v_add_f32_e32 v4, v164, v4
	v_add_f32_e32 v4, v26, v4
	v_add_f32_e32 v4, v165, v4
	v_add_f32_e32 v4, v27, v4
	v_add_f32_e32 v4, v166, v4
	v_add_f32_e32 v4, v28, v4
	s_waitcnt lgkmcnt(0)
	v_mfma_f32_32x32x16_bf16 v[84:99], v[112:115], v[152:155], v[84:99]
	ds_read_b128 v[120:123], v130 offset:31232
	ds_read_b128 v[124:127], v130 offset:26624
	ds_read_b128 v[116:119], v130 offset:26656
	ds_read_b128 v[112:115], v130 offset:31264
	v_add_f32_e32 v4, v29, v4
	v_add_f32_e32 v4, v30, v4
	v_add_f32_e32 v4, v31, v4
	v_add_f32_e32 v4, v32, v4
	v_add_f32_e32 v4, v33, v4
	v_add_f32_e32 v4, v34, v4
	v_add_f32_e32 v167, v35, v4
	v_cvt_pk_bf16_f32 v20, v20, v21
	v_cvt_pk_bf16_f32 v21, v22, v23
	v_cvt_pk_bf16_f32 v22, v24, v25
	v_cvt_pk_bf16_f32 v23, v26, v27
	v_exp_f32_e32 v168, v12
	v_exp_f32_e32 v169, v13
	s_waitcnt lgkmcnt(2)
	v_mfma_f32_32x32x16_bf16 v[36:51], v[124:127], v[20:23], v[36:51]
	v_exp_f32_e32 v170, v14
	v_exp_f32_e32 v171, v15
	v_exp_f32_e32 v172, v16
	v_add_f32_e32 v16, v168, v167
	v_exp_f32_e32 v173, v17
	v_add_f32_e32 v16, v169, v16
	v_cvt_pk_bf16_f32 v24, v28, v29
	v_cvt_pk_bf16_f32 v25, v30, v31
	v_cvt_pk_bf16_f32 v26, v32, v33
	v_cvt_pk_bf16_f32 v27, v34, v35
	v_exp_f32_e32 v174, v18
	v_add_f32_e32 v16, v170, v16
	v_exp_f32_e32 v175, v19
	s_waitcnt lgkmcnt(1)
	v_mfma_f32_32x32x16_bf16 v[36:51], v[116:119], v[24:27], v[36:51]
	v_add_f32_e32 v16, v171, v16
	v_add_f32_e32 v16, v172, v16
	v_add_f32_e32 v16, v173, v16
	v_add_f32_e32 v16, v174, v16
	v_add_f32_e32 v16, v175, v16
	v_cvt_pk_bf16_f32 v14, v163, v164
	v_add_f32_e32 v164, v224, v16
	v_mfma_f32_32x32x16_bf16 v[52:67], v[120:123], v[20:23], v[52:67]
	ds_read_b128 v[4:7], v130 offset:26688
	ds_read_b128 v[156:159], v130 offset:26720
	ds_read_b128 v[8:11], v130 offset:31296
	ds_read_b128 v[108:111], v130 offset:31328
	s_waitcnt vmcnt(2)
	ds_write_b128 v219, v[100:103]
	s_waitcnt vmcnt(1)
	ds_write_b64 v220, v[128:129]
	s_waitcnt vmcnt(0)
	ds_write_b64 v221, v[104:105] offset:35840
	ds_write_b64 v222, v[106:107] offset:35840
	v_cvt_pk_bf16_f32 v12, v131, v160
	v_cvt_pk_bf16_f32 v13, v161, v162
	v_cvt_pk_bf16_f32 v15, v165, v166
	s_waitcnt lgkmcnt(0)
	s_barrier
	v_exp_f32_e32 v120, v68
	v_exp_f32_e32 v122, v69
	v_exp_f32_e32 v126, v70
	v_exp_f32_e32 v131, v71
	s_waitcnt lgkmcnt(7)
	v_mfma_f32_32x32x16_bf16 v[36:51], v[4:7], v[12:15], v[36:51]
	ds_read_b128 v[4:7], v205
	ds_read_b128 v[68:71], v205 offset:32
	s_add_i32 s2, s2, 3
	s_cmp_ge_u32 s2, s34
	v_lshl_add_u32 v124, s1, 7, v204
	s_cselect_b32 s1, s34, 0
	s_sub_i32 s3, s2, s1
	s_cmp_ge_i32 s3, s34
	v_mfma_f32_32x32x16_bf16 v[52:67], v[112:115], v[24:27], v[52:67]
	s_cselect_b32 s3, s34, 0
	s_add_i32 s1, s1, s3
	s_sub_i32 s1, s2, s1
	v_exp_f32_e32 v125, v84
	v_exp_f32_e32 v161, v72
	v_exp_f32_e32 v163, v73
	v_lshl_add_u32 v84, s1, v215, v223
	s_waitcnt lgkmcnt(1)
	v_mfma_f32_32x32x16_bf16 v[20:35], v[4:7], v[132:135], 0
	v_mad_u64_u32 v[72:73], s[2:3], s1, v199, v[202:203]
	v_exp_f32_e32 v121, v85
	v_exp_f32_e32 v123, v86
	v_exp_f32_e32 v127, v87
	ds_read_b128 v[4:7], v205 offset:6656
	ds_read_b128 v[100:103], v205 offset:64
	ds_read_b128 v[112:115], v205 offset:6688
	s_waitcnt lgkmcnt(3)
	v_mfma_f32_32x32x16_bf16 v[20:35], v[68:71], v[136:139], v[20:35]
	global_load_dwordx4 v[84:87], v84, s[44:45]
	s_nop 0
	global_load_dwordx2 v[72:73], v72, s[44:45]
	s_nop 0
	global_load_dwordx4 v[68:71], v124, s[44:45]
	ds_read_b128 v[116:119], v205 offset:6720
	v_cvt_pk_bf16_f32 v104, v168, v169
	v_cvt_pk_bf16_f32 v105, v170, v171
	v_cvt_pk_bf16_f32 v106, v172, v173
	v_cvt_pk_bf16_f32 v107, v174, v175
	v_mfma_f32_32x32x16_bf16 v[52:67], v[8:11], v[12:15], v[52:67]
	v_exp_f32_e32 v160, v88
	v_exp_f32_e32 v162, v89
	v_exp_f32_e32 v124, v90
	v_exp_f32_e32 v128, v74
	v_exp_f32_e32 v74, v91
	v_exp_f32_e32 v129, v75
	v_exp_f32_e32 v75, v92
	s_waitcnt lgkmcnt(3)
	v_mfma_f32_32x32x16_bf16 v[4:19], v[4:7], v[132:135], 0
	v_exp_f32_e32 v165, v97
	v_exp_f32_e32 v166, v98
	v_exp_f32_e32 v167, v99
	s_waitcnt lgkmcnt(1)
	v_mfma_f32_32x32x16_bf16 v[4:19], v[112:115], v[136:139], v[4:19]
	v_mfma_f32_32x32x16_bf16 v[20:35], v[100:103], v[140:143], v[20:35]
	v_add_f32_e32 v100, 0, v125
	v_mfma_f32_32x32x16_bf16 v[36:51], v[156:159], v[104:107], v[36:51]
	v_exp_f32_e32 v156, v93
	v_exp_f32_e32 v157, v94
	v_exp_f32_e32 v158, v95
	ds_read_b128 v[88:91], v205 offset:96
	ds_read_b128 v[92:95], v205 offset:128
	v_exp_f32_e32 v159, v96
	s_waitcnt lgkmcnt(2)
	v_mfma_f32_32x32x16_bf16 v[4:19], v[116:119], v[140:143], v[4:19]
	s_waitcnt lgkmcnt(1)
	v_mfma_f32_32x32x16_bf16 v[20:35], v[88:91], v[144:147], v[20:35]
	ds_read_b128 v[88:91], v205 offset:6752
	ds_read_b128 v[96:99], v205 offset:160
	s_waitcnt lgkmcnt(1)
	v_mfma_f32_32x32x16_bf16 v[4:19], v[88:91], v[144:147], v[4:19]
	v_add_f32_e32 v88, v120, v100
	v_add_f32_e32 v88, v121, v88
	v_add_f32_e32 v88, v122, v88
	v_add_f32_e32 v88, v123, v88
	v_add_f32_e32 v88, v126, v88
	v_add_f32_e32 v88, v127, v88
	v_add_f32_e32 v100, v131, v88
	v_mfma_f32_32x32x16_bf16 v[20:35], v[92:95], v[148:151], v[20:35]
	ds_read_b128 v[88:91], v205 offset:6784
	ds_read_b128 v[92:95], v205 offset:6816
	s_waitcnt lgkmcnt(1)
	v_mfma_f32_32x32x16_bf16 v[4:19], v[88:91], v[148:151], v[4:19]
	v_add_f32_e32 v88, v160, v100
	v_add_f32_e32 v88, v161, v88
	v_add_f32_e32 v88, v162, v88
	v_add_f32_e32 v116, v163, v88
	v_add_f32_e32 v116, v124, v116
	v_add_f32_e32 v116, v128, v116
	v_add_f32_e32 v116, v74, v116
	v_add_f32_e32 v116, v129, v116
	v_mfma_f32_32x32x16_bf16 v[20:35], v[96:99], v[152:155], v[20:35]
	v_add_f32_e32 v116, v75, v116
	v_add_f32_e32 v116, v156, v116
	ds_read_b128 v[88:91], v130 offset:40480
	ds_read_b128 v[100:103], v130 offset:35840
	ds_read_b128 v[112:115], v130 offset:35872
	ds_read_b128 v[96:99], v130 offset:40448
	s_waitcnt lgkmcnt(4)
	v_mfma_f32_32x32x16_bf16 v[4:19], v[92:95], v[152:155], v[4:19]
	v_add_f32_e32 v92, v157, v116
	v_add_f32_e32 v92, v158, v92
	v_add_f32_e32 v92, v159, v92
	v_add_f32_e32 v92, v165, v92
	v_add_f32_e32 v92, v166, v92
	v_add_f32_e32 v116, v167, v92
	v_mfma_f32_32x32x16_bf16 v[52:67], v[108:111], v[104:107], v[52:67]
	v_cvt_pk_bf16_f32 v92, v125, v121
	v_cvt_pk_bf16_f32 v93, v123, v127
	v_cvt_pk_bf16_f32 v94, v160, v162
	v_cvt_pk_bf16_f32 v95, v124, v74
	v_exp_f32_e32 v117, v76
	v_exp_f32_e32 v78, v78
	v_exp_f32_e32 v79, v79
	s_waitcnt lgkmcnt(2)
	v_mfma_f32_32x32x16_bf16 v[36:51], v[100:103], v[92:95], v[36:51]
	v_cvt_pk_bf16_f32 v100, v75, v156
	v_cvt_pk_bf16_f32 v101, v157, v158
	v_cvt_pk_bf16_f32 v102, v159, v165
	v_cvt_pk_bf16_f32 v103, v166, v167
	v_add_f32_e32 v74, v117, v116
	v_cvt_pk_bf16_f32 v75, v126, v131
	v_cvt_pk_bf16_f32 v76, v161, v163
	s_waitcnt lgkmcnt(0)
	v_mfma_f32_32x32x16_bf16 v[52:67], v[96:99], v[92:95], v[52:67]
	ds_read_b128 v[92:95], v130 offset:35904
	ds_read_b128 v[96:99], v130 offset:35936
	ds_read_b128 v[104:107], v130 offset:40512
	ds_read_b128 v[108:111], v130 offset:40544
	v_exp_f32_e32 v80, v80
	v_exp_f32_e32 v81, v81
	v_exp_f32_e32 v82, v82
	v_exp_f32_e32 v83, v83
	s_cmp_ge_u32 s0, s34
	v_mfma_f32_32x32x16_bf16 v[36:51], v[112:115], v[100:103], v[36:51]
	v_exp_f32_e32 v112, v77
	v_cvt_pk_bf16_f32 v77, v128, v129
	s_mov_b32 s1, s0
	v_add_f32_e32 v74, v112, v74
	v_add_f32_e32 v74, v78, v74
	v_mfma_f32_32x32x16_bf16 v[52:67], v[88:91], v[100:103], v[52:67]
	v_add_f32_e32 v88, v79, v74
	v_cvt_pk_bf16_f32 v74, v120, v122
	v_add_f32_e32 v88, v80, v88
	v_add_f32_e32 v88, v81, v88
	v_add_f32_e32 v88, v82, v88
	v_add_f32_e32 v88, v83, v88
	v_add_f32_e32 v224, v164, v88
	s_waitcnt lgkmcnt(3)
	v_mfma_f32_32x32x16_bf16 v[36:51], v[92:95], v[74:77], v[36:51]
	s_waitcnt vmcnt(2)
	ds_write_b128 v219, v[84:87] offset:13312
	s_waitcnt vmcnt(1)
	ds_write_b64 v220, v[72:73] offset:13312
	s_waitcnt vmcnt(0)
	ds_write_b64 v221, v[68:69] offset:26624
	ds_write_b64 v222, v[70:71] offset:26624
	s_waitcnt lgkmcnt(0)
	s_barrier
	s_waitcnt lgkmcnt(5)
	v_mfma_f32_32x32x16_bf16 v[52:67], v[104:107], v[74:77], v[52:67]
	v_cvt_pk_bf16_f32 v74, v117, v112
	v_cvt_pk_bf16_f32 v75, v78, v79
	v_cvt_pk_bf16_f32 v76, v80, v81
	v_cvt_pk_bf16_f32 v77, v82, v83
	s_nop 1
	v_mfma_f32_32x32x16_bf16 v[36:51], v[96:99], v[74:77], v[36:51]
	s_waitcnt lgkmcnt(4)
	v_mfma_f32_32x32x16_bf16 v[52:67], v[108:111], v[74:77], v[52:67]
	s_cbranch_scc0 .LBB0_1139
	s_branch .LBB0_1109
.LBB0_1140:
	s_mov_b32 s0, 0
	v_writelane_b32 v255, s0, 63

.Lprobe_x_end:
	v_readlane_b32 s0, v255, 63
	s_nop 3
	s_add_i32 s0, s0, 1
	v_writelane_b32 v255, s0, 63
	s_cmp_lt_i32 s0, 2
	s_cbranch_scc1 .Lprobe_x_top
